# baseline (speedup 1.0000x reference)
.Lkf_zero_done:
	s_or_b64 exec, exec, s[16:17]
	s_getpc_b64 s[20:21]
.Lkf_pc_here:
	s_add_u32 s20, s20, _Z9k4_reducePKjP15HIP_vector_typeIjLj2EE-.Lkf_pc_here
	s_addc_u32 s21, s21, 0
	v_and_b32_e32 v149, 63, v0
	v_min_u32_e32 v149, 30, v149
	v_lshlrev_b32_e32 v149, 7, v149
	global_load_dword v149, v149, s[20:21]
	v_cmp_ne_u32_e64 s[0:1], 0, v0
	v_cmp_gt_u32_e32 vcc, 48, v0
	s_and_saveexec_b64 s[16:17], vcc
	s_cbranch_execz .Lkf_par_done
	v_lshrrev_b32_e32 v35, 4, v0
	v_and_b32_e32 v36, 15, v0
	v_lshl_add_u32 v37, s24, 4, v36
	v_mad_u32_u24 v37, v37, 3, v35
	v_lshlrev_b32_e32 v38, 5, v37
	v_cmp_eq_u32_e64 s[18:19], s3, v36
	v_lshlrev_b32_e32 v154, 2, v35
	s_mov_b32 s22, 0x40000

.Lkf_par_done:
	s_mov_b64 exec, -1
	v_lshlrev_b32_e32 v4, 16, v4
	v_lshlrev_b32_e32 v5, 24, v5
	v_lshl_or_b32 v3, v3, 8, v4
	v_lshlrev_b32_e32 v4, 16, v12
	v_or3_b32 v3, v3, v5, v2
	v_lshlrev_b32_e32 v5, 24, v13
	v_lshl_or_b32 v4, v11, 8, v4
	v_or3_b32 v43, v4, v5, v10
	v_lshlrev_b32_e32 v4, 16, v16
	v_lshlrev_b32_e32 v5, 24, v17
	v_lshl_or_b32 v4, v15, 8, v4
	v_lshlrev_b32_e32 v8, 16, v8
	v_or3_b32 v42, v4, v5, v14
	v_lshlrev_b32_e32 v4, 16, v20
	v_lshlrev_b32_e32 v9, 24, v9
	v_lshl_or_b32 v7, v7, 8, v8
	v_lshlrev_b32_e32 v5, 24, v21
	v_lshl_or_b32 v4, v19, 8, v4
	v_or3_b32 v44, v7, v9, v6
	v_or3_b32 v41, v4, v5, v18
	v_lshlrev_b32_e32 v4, 16, v24
	v_mov_b32_e32 v7, 0
	v_mov_b32_e32 v8, 0x64c
	v_lshlrev_b32_e32 v5, 24, v25
	v_lshl_or_b32 v4, v23, 8, v4
	s_waitcnt lgkmcnt(0)
	s_barrier
	ds_read_b96 v[36:38], v7 offset:1600
	ds_read_b64 v[16:17], v7 offset:1624
	ds_read2_b32 v[20:21], v8 offset1:1
	v_or3_b32 v19, v4, v5, v22
	v_lshlrev_b32_e32 v4, 16, v28
	v_lshlrev_b32_e32 v5, 24, v29
	v_lshl_or_b32 v4, v27, 8, v4
	v_or3_b32 v13, v4, v5, v26
	v_lshlrev_b32_e32 v4, 16, v32
	v_lshlrev_b32_e32 v5, 24, v33
	v_lshl_or_b32 v4, v31, 8, v4
	v_or3_b32 v9, v4, v5, v30
	ds_read_b32 v8, v7 offset:1620
	ds_read_b32 v12, v7 offset:1632
	ds_read_b128 v[30:33], v134 offset:49152
	s_movk_i32 s3, 0xfff
	v_mov_b32_e32 v11, 0x670
	v_mov_b32_e32 v15, 0x10000
	v_mov_b32_e32 v164, 1
	v_mov_b32_e32 v165, 2
	s_mov_b32 s16, 0xfff0fff0
	s_mov_b32 s17, 1
	s_mov_b32 s18, 2
	s_mov_b32 s19, 3
	s_waitcnt vmcnt(0) lgkmcnt(0)
	v_mov_b32_e32 v24, v38
	v_pk_fma_f32 v[22:23], v[76:77], v[20:21], v[16:17] op_sel_hi:[1,0,0]
	v_pk_fma_f32 v[22:23], v[78:79], v[36:37], v[22:23] op_sel_hi:[1,0,1]
	s_nop 0
	v_exp_f32_e32 v26, v22
	v_exp_f32_e32 v27, v23
	v_pk_fma_f32 v[154:155], v[76:77], v[20:21], v[16:17] op_sel:[0,1,1]
	v_cmp_eq_u32_sdwa vcc, s17, v44 src0_sel:DWORD src1_sel:BYTE_0
	v_pk_fma_f32 v[154:155], v[78:79], v[36:37], v[154:155] op_sel:[0,1,0]
	v_cvt_pknorm_u16_f32 v158, v26, v27
	v_and_b32_e32 v159, s16, v158
	v_exp_f32_e32 v156, v154
	v_cndmask_b32_e32 v162, v164, v15, vcc
	v_cndmask_b32_e32 v150, 0, v26, vcc
	v_exp_f32_e32 v157, v155
	v_cmp_eq_u32_sdwa vcc, s17, v44 src0_sel:DWORD src1_sel:BYTE_1
	v_lshrrev_b32_sdwa v160, v165, v159 dst_sel:DWORD dst_unused:UNUSED_PAD src0_sel:DWORD src1_sel:WORD_0
	v_lshrrev_b32_sdwa v161, v165, v159 dst_sel:DWORD dst_unused:UNUSED_PAD src0_sel:DWORD src1_sel:WORD_1
	v_cndmask_b32_e32 v163, v164, v15, vcc
	v_cndmask_b32_e32 v151, 0, v27, vcc
	ds_add_u32 v160, v162 offset:1648
	ds_add_u32 v161, v163 offset:1648
	v_pk_fma_f32 v[22:23], v[76:77], v[8:9], v[12:13] op_sel_hi:[1,0,0]
	v_cmp_eq_u32_sdwa vcc, s18, v44 src0_sel:DWORD src1_sel:BYTE_0
	v_pk_fma_f32 v[22:23], v[78:79], v[24:25], v[22:23] op_sel_hi:[1,0,1]
	v_cvt_pknorm_u16_f32 v158, v156, v157
	v_and_b32_e32 v159, s16, v158
	v_exp_f32_e32 v26, v22
	v_cndmask_b32_e32 v162, v164, v15, vcc
	v_cndmask_b32_e32 v150, v150, v156, vcc
	v_exp_f32_e32 v27, v23
	v_cmp_eq_u32_sdwa vcc, s18, v44 src0_sel:DWORD src1_sel:BYTE_1
	v_lshrrev_b32_sdwa v160, v165, v159 dst_sel:DWORD dst_unused:UNUSED_PAD src0_sel:DWORD src1_sel:WORD_0
	v_lshrrev_b32_sdwa v161, v165, v159 dst_sel:DWORD dst_unused:UNUSED_PAD src0_sel:DWORD src1_sel:WORD_1
	v_cndmask_b32_e32 v163, v164, v15, vcc
	v_cndmask_b32_e32 v151, v151, v157, vcc
	ds_add_u32 v160, v162 offset:18032
	ds_add_u32 v161, v163 offset:18032
	v_pk_fma_f32 v[154:155], v[80:81], v[20:21], v[16:17] op_sel_hi:[1,0,0]
	v_cmp_eq_u32_sdwa vcc, s19, v44 src0_sel:DWORD src1_sel:BYTE_0
	v_pk_fma_f32 v[154:155], v[82:83], v[36:37], v[154:155] op_sel_hi:[1,0,1]
	v_cvt_pknorm_u16_f32 v158, v26, v27
	v_and_b32_e32 v159, s16, v158
	v_exp_f32_e32 v156, v154
	v_cndmask_b32_e32 v162, v164, v15, vcc
	v_cndmask_b32_e32 v150, v150, v26, vcc
	v_exp_f32_e32 v157, v155
	v_cmp_eq_u32_sdwa vcc, s19, v44 src0_sel:DWORD src1_sel:BYTE_1
	v_lshrrev_b32_sdwa v160, v165, v159 dst_sel:DWORD dst_unused:UNUSED_PAD src0_sel:DWORD src1_sel:WORD_0
	v_lshrrev_b32_sdwa v161, v165, v159 dst_sel:DWORD dst_unused:UNUSED_PAD src0_sel:DWORD src1_sel:WORD_1
	v_cndmask_b32_e32 v163, v164, v15, vcc
	v_cndmask_b32_e32 v151, v151, v27, vcc
	ds_add_u32 v160, v162 offset:34416
	ds_add_u32 v161, v163 offset:34416
	s_waitcnt lgkmcnt(6)
	v_pk_add_f32 v[166:167], v[30:31], v[150:151] neg_lo:[0,1] neg_hi:[0,1]
	s_nop 0
	v_pk_mul_f32 v[166:167], v[166:167], v[166:167]
	v_pk_fma_f32 v[22:23], v[80:81], v[20:21], v[16:17] op_sel:[0,1,1]
	v_cmp_eq_u32_sdwa vcc, s17, v44 src0_sel:DWORD src1_sel:BYTE_2
	v_pk_fma_f32 v[22:23], v[82:83], v[36:37], v[22:23] op_sel:[0,1,0]
	v_cvt_pknorm_u16_f32 v158, v156, v157
	v_and_b32_e32 v159, s16, v158
	v_exp_f32_e32 v26, v22
	v_cndmask_b32_e32 v162, v164, v15, vcc
	v_cndmask_b32_e32 v152, 0, v156, vcc
	v_exp_f32_e32 v27, v23
	v_cmp_eq_u32_sdwa vcc, s17, v44 src0_sel:DWORD src1_sel:BYTE_3
	v_lshrrev_b32_sdwa v160, v165, v159 dst_sel:DWORD dst_unused:UNUSED_PAD src0_sel:DWORD src1_sel:WORD_0
	v_lshrrev_b32_sdwa v161, v165, v159 dst_sel:DWORD dst_unused:UNUSED_PAD src0_sel:DWORD src1_sel:WORD_1
	v_cndmask_b32_e32 v163, v164, v15, vcc
	v_cndmask_b32_e32 v153, 0, v157, vcc
	ds_add_u32 v160, v162 offset:1648
	ds_add_u32 v161, v163 offset:1648
	v_pk_fma_f32 v[154:155], v[80:81], v[8:9], v[12:13] op_sel_hi:[1,0,0]
	v_cmp_eq_u32_sdwa vcc, s18, v44 src0_sel:DWORD src1_sel:BYTE_2
	v_pk_fma_f32 v[154:155], v[82:83], v[24:25], v[154:155] op_sel_hi:[1,0,1]
	v_cvt_pknorm_u16_f32 v158, v26, v27
	v_and_b32_e32 v159, s16, v158
	v_exp_f32_e32 v156, v154
	v_cndmask_b32_e32 v162, v164, v15, vcc
	v_cndmask_b32_e32 v152, v152, v26, vcc
	v_exp_f32_e32 v157, v155
	v_cmp_eq_u32_sdwa vcc, s18, v44 src0_sel:DWORD src1_sel:BYTE_3
	v_lshrrev_b32_sdwa v160, v165, v159 dst_sel:DWORD dst_unused:UNUSED_PAD src0_sel:DWORD src1_sel:WORD_0
	v_lshrrev_b32_sdwa v161, v165, v159 dst_sel:DWORD dst_unused:UNUSED_PAD src0_sel:DWORD src1_sel:WORD_1
	v_cndmask_b32_e32 v163, v164, v15, vcc
	v_cndmask_b32_e32 v153, v153, v27, vcc
	ds_add_u32 v160, v162 offset:18032
	ds_add_u32 v161, v163 offset:18032
	v_cmp_eq_u32_sdwa vcc, s19, v44 src0_sel:DWORD src1_sel:BYTE_2
	s_nop 0
	v_cvt_pknorm_u16_f32 v158, v156, v157
	v_and_b32_e32 v159, s16, v158
	v_cndmask_b32_e32 v162, v164, v15, vcc
	v_cndmask_b32_e32 v152, v152, v156, vcc
	v_cmp_eq_u32_sdwa vcc, s19, v44 src0_sel:DWORD src1_sel:BYTE_3
	v_lshrrev_b32_sdwa v160, v165, v159 dst_sel:DWORD dst_unused:UNUSED_PAD src0_sel:DWORD src1_sel:WORD_0
	v_lshrrev_b32_sdwa v161, v165, v159 dst_sel:DWORD dst_unused:UNUSED_PAD src0_sel:DWORD src1_sel:WORD_1
	v_cndmask_b32_e32 v163, v164, v15, vcc
	v_cndmask_b32_e32 v153, v153, v157, vcc
	ds_add_u32 v160, v162 offset:34416
	ds_add_u32 v161, v163 offset:34416
	v_pk_add_f32 v[22:23], v[32:33], v[152:153] neg_lo:[0,1] neg_hi:[0,1]
	s_nop 0
	v_pk_fma_f32 v[28:29], v[22:23], v[22:23], v[166:167]
	ds_read_b128 v[76:79], v134 offset:61440
	v_pk_fma_f32 v[80:81], v[84:85], v[20:21], v[16:17] op_sel_hi:[1,0,0]
	v_pk_fma_f32 v[80:81], v[86:87], v[36:37], v[80:81] op_sel_hi:[1,0,1]
	s_nop 0
	v_exp_f32_e32 v82, v80
	v_exp_f32_e32 v83, v81
	v_pk_fma_f32 v[154:155], v[84:85], v[20:21], v[16:17] op_sel:[0,1,1]
	v_cmp_eq_u32_sdwa vcc, s17, v3 src0_sel:DWORD src1_sel:BYTE_0
	v_pk_fma_f32 v[154:155], v[86:87], v[36:37], v[154:155] op_sel:[0,1,0]
	v_cvt_pknorm_u16_f32 v158, v82, v83
	v_and_b32_e32 v159, s16, v158
	v_exp_f32_e32 v156, v154
	v_cndmask_b32_e32 v162, v164, v15, vcc
	v_cndmask_b32_e32 v150, 0, v82, vcc
	v_exp_f32_e32 v157, v155
	v_cmp_eq_u32_sdwa vcc, s17, v3 src0_sel:DWORD src1_sel:BYTE_1
	v_lshrrev_b32_sdwa v160, v165, v159 dst_sel:DWORD dst_unused:UNUSED_PAD src0_sel:DWORD src1_sel:WORD_0
	v_lshrrev_b32_sdwa v161, v165, v159 dst_sel:DWORD dst_unused:UNUSED_PAD src0_sel:DWORD src1_sel:WORD_1
	v_cndmask_b32_e32 v163, v164, v15, vcc
	v_cndmask_b32_e32 v151, 0, v83, vcc
	ds_add_u32 v160, v162 offset:1648
	ds_add_u32 v161, v163 offset:1648
	v_pk_fma_f32 v[80:81], v[84:85], v[8:9], v[12:13] op_sel_hi:[1,0,0]
	v_cmp_eq_u32_sdwa vcc, s18, v3 src0_sel:DWORD src1_sel:BYTE_0
	v_pk_fma_f32 v[80:81], v[86:87], v[24:25], v[80:81] op_sel_hi:[1,0,1]
	v_cvt_pknorm_u16_f32 v158, v156, v157
	v_and_b32_e32 v159, s16, v158
	v_exp_f32_e32 v82, v80
	v_cndmask_b32_e32 v162, v164, v15, vcc
	v_cndmask_b32_e32 v150, v150, v156, vcc
	v_exp_f32_e32 v83, v81
	v_cmp_eq_u32_sdwa vcc, s18, v3 src0_sel:DWORD src1_sel:BYTE_1
	v_lshrrev_b32_sdwa v160, v165, v159 dst_sel:DWORD dst_unused:UNUSED_PAD src0_sel:DWORD src1_sel:WORD_0
	v_lshrrev_b32_sdwa v161, v165, v159 dst_sel:DWORD dst_unused:UNUSED_PAD src0_sel:DWORD src1_sel:WORD_1
	v_cndmask_b32_e32 v163, v164, v15, vcc
	v_cndmask_b32_e32 v151, v151, v157, vcc
	ds_add_u32 v160, v162 offset:18032
	ds_add_u32 v161, v163 offset:18032
	v_pk_fma_f32 v[154:155], v[88:89], v[20:21], v[16:17] op_sel_hi:[1,0,0]
	v_cmp_eq_u32_sdwa vcc, s19, v3 src0_sel:DWORD src1_sel:BYTE_0
	v_pk_fma_f32 v[154:155], v[90:91], v[36:37], v[154:155] op_sel_hi:[1,0,1]
	v_cvt_pknorm_u16_f32 v158, v82, v83
	v_and_b32_e32 v159, s16, v158
	v_exp_f32_e32 v156, v154
	v_cndmask_b32_e32 v162, v164, v15, vcc
	v_cndmask_b32_e32 v150, v150, v82, vcc
	v_exp_f32_e32 v157, v155
	v_cmp_eq_u32_sdwa vcc, s19, v3 src0_sel:DWORD src1_sel:BYTE_1
	v_lshrrev_b32_sdwa v160, v165, v159 dst_sel:DWORD dst_unused:UNUSED_PAD src0_sel:DWORD src1_sel:WORD_0
	v_lshrrev_b32_sdwa v161, v165, v159 dst_sel:DWORD dst_unused:UNUSED_PAD src0_sel:DWORD src1_sel:WORD_1
	v_cndmask_b32_e32 v163, v164, v15, vcc
	v_cndmask_b32_e32 v151, v151, v83, vcc
	ds_add_u32 v160, v162 offset:34416
	ds_add_u32 v161, v163 offset:34416
	s_waitcnt lgkmcnt(6)
	v_pk_add_f32 v[166:167], v[76:77], v[150:151] neg_lo:[0,1] neg_hi:[0,1]
	s_nop 0
	v_pk_fma_f32 v[166:167], v[166:167], v[166:167], v[28:29]
	v_pk_fma_f32 v[80:81], v[88:89], v[20:21], v[16:17] op_sel:[0,1,1]
	v_cmp_eq_u32_sdwa vcc, s17, v3 src0_sel:DWORD src1_sel:BYTE_2
	v_pk_fma_f32 v[80:81], v[90:91], v[36:37], v[80:81] op_sel:[0,1,0]
	v_cvt_pknorm_u16_f32 v158, v156, v157
	v_and_b32_e32 v159, s16, v158
	v_exp_f32_e32 v82, v80
	v_cndmask_b32_e32 v162, v164, v15, vcc
	v_cndmask_b32_e32 v152, 0, v156, vcc
	v_exp_f32_e32 v83, v81
	v_cmp_eq_u32_sdwa vcc, s17, v3 src0_sel:DWORD src1_sel:BYTE_3
	v_lshrrev_b32_sdwa v160, v165, v159 dst_sel:DWORD dst_unused:UNUSED_PAD src0_sel:DWORD src1_sel:WORD_0
	v_lshrrev_b32_sdwa v161, v165, v159 dst_sel:DWORD dst_unused:UNUSED_PAD src0_sel:DWORD src1_sel:WORD_1
	v_cndmask_b32_e32 v163, v164, v15, vcc
	v_cndmask_b32_e32 v153, 0, v157, vcc
	ds_add_u32 v160, v162 offset:1648
	ds_add_u32 v161, v163 offset:1648
	v_pk_fma_f32 v[154:155], v[88:89], v[8:9], v[12:13] op_sel_hi:[1,0,0]
	v_cmp_eq_u32_sdwa vcc, s18, v3 src0_sel:DWORD src1_sel:BYTE_2
	v_pk_fma_f32 v[154:155], v[90:91], v[24:25], v[154:155] op_sel_hi:[1,0,1]
	v_cvt_pknorm_u16_f32 v158, v82, v83
	v_and_b32_e32 v159, s16, v158
	v_exp_f32_e32 v156, v154
	v_cndmask_b32_e32 v162, v164, v15, vcc
	v_cndmask_b32_e32 v152, v152, v82, vcc
	v_exp_f32_e32 v157, v155
	v_cmp_eq_u32_sdwa vcc, s18, v3 src0_sel:DWORD src1_sel:BYTE_3
	v_lshrrev_b32_sdwa v160, v165, v159 dst_sel:DWORD dst_unused:UNUSED_PAD src0_sel:DWORD src1_sel:WORD_0
	v_lshrrev_b32_sdwa v161, v165, v159 dst_sel:DWORD dst_unused:UNUSED_PAD src0_sel:DWORD src1_sel:WORD_1
	v_cndmask_b32_e32 v163, v164, v15, vcc
	v_cndmask_b32_e32 v153, v153, v83, vcc
	ds_add_u32 v160, v162 offset:18032
	ds_add_u32 v161, v163 offset:18032
	v_cmp_eq_u32_sdwa vcc, s19, v3 src0_sel:DWORD src1_sel:BYTE_2
	s_nop 0
	v_cvt_pknorm_u16_f32 v158, v156, v157
	v_and_b32_e32 v159, s16, v158
	v_cndmask_b32_e32 v162, v164, v15, vcc
	v_cndmask_b32_e32 v152, v152, v156, vcc
	v_cmp_eq_u32_sdwa vcc, s19, v3 src0_sel:DWORD src1_sel:BYTE_3
	v_lshrrev_b32_sdwa v160, v165, v159 dst_sel:DWORD dst_unused:UNUSED_PAD src0_sel:DWORD src1_sel:WORD_0
	v_lshrrev_b32_sdwa v161, v165, v159 dst_sel:DWORD dst_unused:UNUSED_PAD src0_sel:DWORD src1_sel:WORD_1
	v_cndmask_b32_e32 v163, v164, v15, vcc
	v_cndmask_b32_e32 v153, v153, v157, vcc
	ds_add_u32 v160, v162 offset:34416
	ds_add_u32 v161, v163 offset:34416
	v_pk_add_f32 v[80:81], v[78:79], v[152:153] neg_lo:[0,1] neg_hi:[0,1]
	s_nop 0
	v_pk_fma_f32 v[6:7], v[80:81], v[80:81], v[166:167]
	ds_read_b128 v[76:79], v1 offset:24576
	v_pk_fma_f32 v[80:81], v[92:93], v[20:21], v[16:17] op_sel_hi:[1,0,0]
	v_pk_fma_f32 v[80:81], v[94:95], v[36:37], v[80:81] op_sel_hi:[1,0,1]
	s_nop 0
	v_exp_f32_e32 v82, v80
	v_exp_f32_e32 v83, v81
	v_pk_fma_f32 v[154:155], v[92:93], v[20:21], v[16:17] op_sel:[0,1,1]
	v_cmp_eq_u32_sdwa vcc, s17, v43 src0_sel:DWORD src1_sel:BYTE_0
	v_pk_fma_f32 v[154:155], v[94:95], v[36:37], v[154:155] op_sel:[0,1,0]
	v_cvt_pknorm_u16_f32 v158, v82, v83
	v_and_b32_e32 v159, s16, v158
	v_exp_f32_e32 v156, v154
	v_cndmask_b32_e32 v162, v164, v15, vcc
	v_cndmask_b32_e32 v150, 0, v82, vcc
	v_exp_f32_e32 v157, v155
	v_cmp_eq_u32_sdwa vcc, s17, v43 src0_sel:DWORD src1_sel:BYTE_1
	v_lshrrev_b32_sdwa v160, v165, v159 dst_sel:DWORD dst_unused:UNUSED_PAD src0_sel:DWORD src1_sel:WORD_0
	v_lshrrev_b32_sdwa v161, v165, v159 dst_sel:DWORD dst_unused:UNUSED_PAD src0_sel:DWORD src1_sel:WORD_1
	v_cndmask_b32_e32 v163, v164, v15, vcc
	v_cndmask_b32_e32 v151, 0, v83, vcc
	ds_add_u32 v160, v162 offset:1648
	ds_add_u32 v161, v163 offset:1648
	v_pk_fma_f32 v[80:81], v[92:93], v[8:9], v[12:13] op_sel_hi:[1,0,0]
	v_cmp_eq_u32_sdwa vcc, s18, v43 src0_sel:DWORD src1_sel:BYTE_0
	v_pk_fma_f32 v[80:81], v[94:95], v[24:25], v[80:81] op_sel_hi:[1,0,1]
	v_cvt_pknorm_u16_f32 v158, v156, v157
	v_and_b32_e32 v159, s16, v158
	v_exp_f32_e32 v82, v80
	v_cndmask_b32_e32 v162, v164, v15, vcc
	v_cndmask_b32_e32 v150, v150, v156, vcc
	v_exp_f32_e32 v83, v81
	v_cmp_eq_u32_sdwa vcc, s18, v43 src0_sel:DWORD src1_sel:BYTE_1
	v_lshrrev_b32_sdwa v160, v165, v159 dst_sel:DWORD dst_unused:UNUSED_PAD src0_sel:DWORD src1_sel:WORD_0
	v_lshrrev_b32_sdwa v161, v165, v159 dst_sel:DWORD dst_unused:UNUSED_PAD src0_sel:DWORD src1_sel:WORD_1
	v_cndmask_b32_e32 v163, v164, v15, vcc
	v_cndmask_b32_e32 v151, v151, v157, vcc
	ds_add_u32 v160, v162 offset:18032
	ds_add_u32 v161, v163 offset:18032
	v_pk_fma_f32 v[154:155], v[96:97], v[20:21], v[16:17] op_sel_hi:[1,0,0]
	v_cmp_eq_u32_sdwa vcc, s19, v43 src0_sel:DWORD src1_sel:BYTE_0
	v_pk_fma_f32 v[154:155], v[98:99], v[36:37], v[154:155] op_sel_hi:[1,0,1]
	v_cvt_pknorm_u16_f32 v158, v82, v83
	v_and_b32_e32 v159, s16, v158
	v_exp_f32_e32 v156, v154
	v_cndmask_b32_e32 v162, v164, v15, vcc
	v_cndmask_b32_e32 v150, v150, v82, vcc
	v_exp_f32_e32 v157, v155
	v_cmp_eq_u32_sdwa vcc, s19, v43 src0_sel:DWORD src1_sel:BYTE_1
	v_lshrrev_b32_sdwa v160, v165, v159 dst_sel:DWORD dst_unused:UNUSED_PAD src0_sel:DWORD src1_sel:WORD_0
	v_lshrrev_b32_sdwa v161, v165, v159 dst_sel:DWORD dst_unused:UNUSED_PAD src0_sel:DWORD src1_sel:WORD_1
	v_cndmask_b32_e32 v163, v164, v15, vcc
	v_cndmask_b32_e32 v151, v151, v83, vcc
	ds_add_u32 v160, v162 offset:34416
	ds_add_u32 v161, v163 offset:34416
	s_waitcnt lgkmcnt(6)
	v_pk_add_f32 v[166:167], v[76:77], v[150:151] neg_lo:[0,1] neg_hi:[0,1]
	s_nop 0
	v_pk_fma_f32 v[166:167], v[166:167], v[166:167], v[6:7]
	v_pk_fma_f32 v[80:81], v[96:97], v[20:21], v[16:17] op_sel:[0,1,1]
	v_cmp_eq_u32_sdwa vcc, s17, v43 src0_sel:DWORD src1_sel:BYTE_2
	v_pk_fma_f32 v[80:81], v[98:99], v[36:37], v[80:81] op_sel:[0,1,0]
	v_cvt_pknorm_u16_f32 v158, v156, v157
	v_and_b32_e32 v159, s16, v158
	v_exp_f32_e32 v82, v80
	v_cndmask_b32_e32 v162, v164, v15, vcc
	v_cndmask_b32_e32 v152, 0, v156, vcc
	v_exp_f32_e32 v83, v81
	v_cmp_eq_u32_sdwa vcc, s17, v43 src0_sel:DWORD src1_sel:BYTE_3
	v_lshrrev_b32_sdwa v160, v165, v159 dst_sel:DWORD dst_unused:UNUSED_PAD src0_sel:DWORD src1_sel:WORD_0
	v_lshrrev_b32_sdwa v161, v165, v159 dst_sel:DWORD dst_unused:UNUSED_PAD src0_sel:DWORD src1_sel:WORD_1
	v_cndmask_b32_e32 v163, v164, v15, vcc
	v_cndmask_b32_e32 v153, 0, v157, vcc
	ds_add_u32 v160, v162 offset:1648
	ds_add_u32 v161, v163 offset:1648
	v_pk_fma_f32 v[154:155], v[96:97], v[8:9], v[12:13] op_sel_hi:[1,0,0]
	v_cmp_eq_u32_sdwa vcc, s18, v43 src0_sel:DWORD src1_sel:BYTE_2
	v_pk_fma_f32 v[154:155], v[98:99], v[24:25], v[154:155] op_sel_hi:[1,0,1]
	v_cvt_pknorm_u16_f32 v158, v82, v83
	v_and_b32_e32 v159, s16, v158
	v_exp_f32_e32 v156, v154
	v_cndmask_b32_e32 v162, v164, v15, vcc
	v_cndmask_b32_e32 v152, v152, v82, vcc
	v_exp_f32_e32 v157, v155
	v_cmp_eq_u32_sdwa vcc, s18, v43 src0_sel:DWORD src1_sel:BYTE_3
	v_lshrrev_b32_sdwa v160, v165, v159 dst_sel:DWORD dst_unused:UNUSED_PAD src0_sel:DWORD src1_sel:WORD_0
	v_lshrrev_b32_sdwa v161, v165, v159 dst_sel:DWORD dst_unused:UNUSED_PAD src0_sel:DWORD src1_sel:WORD_1
	v_cndmask_b32_e32 v163, v164, v15, vcc
	v_cndmask_b32_e32 v153, v153, v83, vcc
	ds_add_u32 v160, v162 offset:18032
	ds_add_u32 v161, v163 offset:18032
	v_cmp_eq_u32_sdwa vcc, s19, v43 src0_sel:DWORD src1_sel:BYTE_2
	s_nop 0
	v_cvt_pknorm_u16_f32 v158, v156, v157
	v_and_b32_e32 v159, s16, v158
	v_cndmask_b32_e32 v162, v164, v15, vcc
	v_cndmask_b32_e32 v152, v152, v156, vcc
	v_cmp_eq_u32_sdwa vcc, s19, v43 src0_sel:DWORD src1_sel:BYTE_3
	v_lshrrev_b32_sdwa v160, v165, v159 dst_sel:DWORD dst_unused:UNUSED_PAD src0_sel:DWORD src1_sel:WORD_0
	v_lshrrev_b32_sdwa v161, v165, v159 dst_sel:DWORD dst_unused:UNUSED_PAD src0_sel:DWORD src1_sel:WORD_1
	v_cndmask_b32_e32 v163, v164, v15, vcc
	v_cndmask_b32_e32 v153, v153, v157, vcc
	ds_add_u32 v160, v162 offset:34416
	ds_add_u32 v161, v163 offset:34416
	v_pk_add_f32 v[80:81], v[78:79], v[152:153] neg_lo:[0,1] neg_hi:[0,1]
	s_nop 0
	v_pk_fma_f32 v[6:7], v[80:81], v[80:81], v[166:167]
	ds_read_b128 v[76:79], v1 offset:36864
	v_pk_fma_f32 v[80:81], v[100:101], v[20:21], v[16:17] op_sel_hi:[1,0,0]
	v_pk_fma_f32 v[80:81], v[102:103], v[36:37], v[80:81] op_sel_hi:[1,0,1]
	s_nop 0
	v_exp_f32_e32 v82, v80
	v_exp_f32_e32 v83, v81
	v_pk_fma_f32 v[154:155], v[100:101], v[20:21], v[16:17] op_sel:[0,1,1]
	v_cmp_eq_u32_sdwa vcc, s17, v42 src0_sel:DWORD src1_sel:BYTE_0
	v_pk_fma_f32 v[154:155], v[102:103], v[36:37], v[154:155] op_sel:[0,1,0]
	v_cvt_pknorm_u16_f32 v158, v82, v83
	v_and_b32_e32 v159, s16, v158
	v_exp_f32_e32 v156, v154
	v_cndmask_b32_e32 v162, v164, v15, vcc
	v_cndmask_b32_e32 v150, 0, v82, vcc
	v_exp_f32_e32 v157, v155
	v_cmp_eq_u32_sdwa vcc, s17, v42 src0_sel:DWORD src1_sel:BYTE_1
	v_lshrrev_b32_sdwa v160, v165, v159 dst_sel:DWORD dst_unused:UNUSED_PAD src0_sel:DWORD src1_sel:WORD_0
	v_lshrrev_b32_sdwa v161, v165, v159 dst_sel:DWORD dst_unused:UNUSED_PAD src0_sel:DWORD src1_sel:WORD_1
	v_cndmask_b32_e32 v163, v164, v15, vcc
	v_cndmask_b32_e32 v151, 0, v83, vcc
	ds_add_u32 v160, v162 offset:1648
	ds_add_u32 v161, v163 offset:1648
	v_pk_fma_f32 v[80:81], v[100:101], v[8:9], v[12:13] op_sel_hi:[1,0,0]
	v_cmp_eq_u32_sdwa vcc, s18, v42 src0_sel:DWORD src1_sel:BYTE_0
	v_pk_fma_f32 v[80:81], v[102:103], v[24:25], v[80:81] op_sel_hi:[1,0,1]
	v_cvt_pknorm_u16_f32 v158, v156, v157
	v_and_b32_e32 v159, s16, v158
	v_exp_f32_e32 v82, v80
	v_cndmask_b32_e32 v162, v164, v15, vcc
	v_cndmask_b32_e32 v150, v150, v156, vcc
	v_exp_f32_e32 v83, v81
	v_cmp_eq_u32_sdwa vcc, s18, v42 src0_sel:DWORD src1_sel:BYTE_1
	v_lshrrev_b32_sdwa v160, v165, v159 dst_sel:DWORD dst_unused:UNUSED_PAD src0_sel:DWORD src1_sel:WORD_0
	v_lshrrev_b32_sdwa v161, v165, v159 dst_sel:DWORD dst_unused:UNUSED_PAD src0_sel:DWORD src1_sel:WORD_1
	v_cndmask_b32_e32 v163, v164, v15, vcc
	v_cndmask_b32_e32 v151, v151, v157, vcc
	ds_add_u32 v160, v162 offset:18032
	ds_add_u32 v161, v163 offset:18032
	v_pk_fma_f32 v[154:155], v[104:105], v[20:21], v[16:17] op_sel_hi:[1,0,0]
	v_cmp_eq_u32_sdwa vcc, s19, v42 src0_sel:DWORD src1_sel:BYTE_0
	v_pk_fma_f32 v[154:155], v[106:107], v[36:37], v[154:155] op_sel_hi:[1,0,1]
	v_cvt_pknorm_u16_f32 v158, v82, v83
	v_and_b32_e32 v159, s16, v158
	v_exp_f32_e32 v156, v154
	v_cndmask_b32_e32 v162, v164, v15, vcc
	v_cndmask_b32_e32 v150, v150, v82, vcc
	v_exp_f32_e32 v157, v155
	v_cmp_eq_u32_sdwa vcc, s19, v42 src0_sel:DWORD src1_sel:BYTE_1
	v_lshrrev_b32_sdwa v160, v165, v159 dst_sel:DWORD dst_unused:UNUSED_PAD src0_sel:DWORD src1_sel:WORD_0
	v_lshrrev_b32_sdwa v161, v165, v159 dst_sel:DWORD dst_unused:UNUSED_PAD src0_sel:DWORD src1_sel:WORD_1
	v_cndmask_b32_e32 v163, v164, v15, vcc
	v_cndmask_b32_e32 v151, v151, v83, vcc
	ds_add_u32 v160, v162 offset:34416
	ds_add_u32 v161, v163 offset:34416
	s_waitcnt lgkmcnt(6)
	v_pk_add_f32 v[166:167], v[76:77], v[150:151] neg_lo:[0,1] neg_hi:[0,1]
	s_nop 0
	v_pk_fma_f32 v[166:167], v[166:167], v[166:167], v[6:7]
	v_pk_fma_f32 v[80:81], v[104:105], v[20:21], v[16:17] op_sel:[0,1,1]
	v_cmp_eq_u32_sdwa vcc, s17, v42 src0_sel:DWORD src1_sel:BYTE_2
	v_pk_fma_f32 v[80:81], v[106:107], v[36:37], v[80:81] op_sel:[0,1,0]
	v_cvt_pknorm_u16_f32 v158, v156, v157
	v_and_b32_e32 v159, s16, v158
	v_exp_f32_e32 v82, v80
	v_cndmask_b32_e32 v162, v164, v15, vcc
	v_cndmask_b32_e32 v152, 0, v156, vcc
	v_exp_f32_e32 v83, v81
	v_cmp_eq_u32_sdwa vcc, s17, v42 src0_sel:DWORD src1_sel:BYTE_3
	v_lshrrev_b32_sdwa v160, v165, v159 dst_sel:DWORD dst_unused:UNUSED_PAD src0_sel:DWORD src1_sel:WORD_0
	v_lshrrev_b32_sdwa v161, v165, v159 dst_sel:DWORD dst_unused:UNUSED_PAD src0_sel:DWORD src1_sel:WORD_1
	v_cndmask_b32_e32 v163, v164, v15, vcc
	v_cndmask_b32_e32 v153, 0, v157, vcc
	ds_add_u32 v160, v162 offset:1648
	ds_add_u32 v161, v163 offset:1648
	v_pk_fma_f32 v[154:155], v[104:105], v[8:9], v[12:13] op_sel_hi:[1,0,0]
	v_cmp_eq_u32_sdwa vcc, s18, v42 src0_sel:DWORD src1_sel:BYTE_2
	v_pk_fma_f32 v[154:155], v[106:107], v[24:25], v[154:155] op_sel_hi:[1,0,1]
	v_cvt_pknorm_u16_f32 v158, v82, v83
	v_and_b32_e32 v159, s16, v158
	v_exp_f32_e32 v156, v154
	v_cndmask_b32_e32 v162, v164, v15, vcc
	v_cndmask_b32_e32 v152, v152, v82, vcc
	v_exp_f32_e32 v157, v155
	v_cmp_eq_u32_sdwa vcc, s18, v42 src0_sel:DWORD src1_sel:BYTE_3
	v_lshrrev_b32_sdwa v160, v165, v159 dst_sel:DWORD dst_unused:UNUSED_PAD src0_sel:DWORD src1_sel:WORD_0
	v_lshrrev_b32_sdwa v161, v165, v159 dst_sel:DWORD dst_unused:UNUSED_PAD src0_sel:DWORD src1_sel:WORD_1
	v_cndmask_b32_e32 v163, v164, v15, vcc
	v_cndmask_b32_e32 v153, v153, v83, vcc
	ds_add_u32 v160, v162 offset:18032
	ds_add_u32 v161, v163 offset:18032
	v_cmp_eq_u32_sdwa vcc, s19, v42 src0_sel:DWORD src1_sel:BYTE_2
	s_nop 0
	v_cvt_pknorm_u16_f32 v158, v156, v157
	v_and_b32_e32 v159, s16, v158
	v_cndmask_b32_e32 v162, v164, v15, vcc
	v_cndmask_b32_e32 v152, v152, v156, vcc
	v_cmp_eq_u32_sdwa vcc, s19, v42 src0_sel:DWORD src1_sel:BYTE_3
	v_lshrrev_b32_sdwa v160, v165, v159 dst_sel:DWORD dst_unused:UNUSED_PAD src0_sel:DWORD src1_sel:WORD_0
	v_lshrrev_b32_sdwa v161, v165, v159 dst_sel:DWORD dst_unused:UNUSED_PAD src0_sel:DWORD src1_sel:WORD_1
	v_cndmask_b32_e32 v163, v164, v15, vcc
	v_cndmask_b32_e32 v153, v153, v157, vcc
	ds_add_u32 v160, v162 offset:34416
	ds_add_u32 v161, v163 offset:34416
	v_pk_add_f32 v[80:81], v[78:79], v[152:153] neg_lo:[0,1] neg_hi:[0,1]
	s_nop 0
	v_pk_fma_f32 v[6:7], v[80:81], v[80:81], v[166:167]
	ds_read_b128 v[76:79], v1 offset:49152
	v_pk_fma_f32 v[80:81], v[108:109], v[20:21], v[16:17] op_sel_hi:[1,0,0]
	v_pk_fma_f32 v[80:81], v[110:111], v[36:37], v[80:81] op_sel_hi:[1,0,1]
	s_nop 0
	v_exp_f32_e32 v82, v80
	v_exp_f32_e32 v83, v81
	v_pk_fma_f32 v[154:155], v[108:109], v[20:21], v[16:17] op_sel:[0,1,1]
	v_cmp_eq_u32_sdwa vcc, s17, v41 src0_sel:DWORD src1_sel:BYTE_0
	v_pk_fma_f32 v[154:155], v[110:111], v[36:37], v[154:155] op_sel:[0,1,0]
	v_cvt_pknorm_u16_f32 v158, v82, v83
	v_and_b32_e32 v159, s16, v158
	v_exp_f32_e32 v156, v154
	v_cndmask_b32_e32 v162, v164, v15, vcc
	v_cndmask_b32_e32 v150, 0, v82, vcc
	v_exp_f32_e32 v157, v155
	v_cmp_eq_u32_sdwa vcc, s17, v41 src0_sel:DWORD src1_sel:BYTE_1
	v_lshrrev_b32_sdwa v160, v165, v159 dst_sel:DWORD dst_unused:UNUSED_PAD src0_sel:DWORD src1_sel:WORD_0
	v_lshrrev_b32_sdwa v161, v165, v159 dst_sel:DWORD dst_unused:UNUSED_PAD src0_sel:DWORD src1_sel:WORD_1
	v_cndmask_b32_e32 v163, v164, v15, vcc
	v_cndmask_b32_e32 v151, 0, v83, vcc
	ds_add_u32 v160, v162 offset:1648
	ds_add_u32 v161, v163 offset:1648
	v_pk_fma_f32 v[80:81], v[108:109], v[8:9], v[12:13] op_sel_hi:[1,0,0]
	v_cmp_eq_u32_sdwa vcc, s18, v41 src0_sel:DWORD src1_sel:BYTE_0
	v_pk_fma_f32 v[80:81], v[110:111], v[24:25], v[80:81] op_sel_hi:[1,0,1]
	v_cvt_pknorm_u16_f32 v158, v156, v157
	v_and_b32_e32 v159, s16, v158
	v_exp_f32_e32 v82, v80
	v_cndmask_b32_e32 v162, v164, v15, vcc
	v_cndmask_b32_e32 v150, v150, v156, vcc
	v_exp_f32_e32 v83, v81
	v_cmp_eq_u32_sdwa vcc, s18, v41 src0_sel:DWORD src1_sel:BYTE_1
	v_lshrrev_b32_sdwa v160, v165, v159 dst_sel:DWORD dst_unused:UNUSED_PAD src0_sel:DWORD src1_sel:WORD_0
	v_lshrrev_b32_sdwa v161, v165, v159 dst_sel:DWORD dst_unused:UNUSED_PAD src0_sel:DWORD src1_sel:WORD_1
	v_cndmask_b32_e32 v163, v164, v15, vcc
	v_cndmask_b32_e32 v151, v151, v157, vcc
	ds_add_u32 v160, v162 offset:18032
	ds_add_u32 v161, v163 offset:18032
	v_pk_fma_f32 v[154:155], v[112:113], v[20:21], v[16:17] op_sel_hi:[1,0,0]
	v_cmp_eq_u32_sdwa vcc, s19, v41 src0_sel:DWORD src1_sel:BYTE_0
	v_pk_fma_f32 v[154:155], v[114:115], v[36:37], v[154:155] op_sel_hi:[1,0,1]
	v_cvt_pknorm_u16_f32 v158, v82, v83
	v_and_b32_e32 v159, s16, v158
	v_exp_f32_e32 v156, v154
	v_cndmask_b32_e32 v162, v164, v15, vcc
	v_cndmask_b32_e32 v150, v150, v82, vcc
	v_exp_f32_e32 v157, v155
	v_cmp_eq_u32_sdwa vcc, s19, v41 src0_sel:DWORD src1_sel:BYTE_1
	v_lshrrev_b32_sdwa v160, v165, v159 dst_sel:DWORD dst_unused:UNUSED_PAD src0_sel:DWORD src1_sel:WORD_0
	v_lshrrev_b32_sdwa v161, v165, v159 dst_sel:DWORD dst_unused:UNUSED_PAD src0_sel:DWORD src1_sel:WORD_1
	v_cndmask_b32_e32 v163, v164, v15, vcc
	v_cndmask_b32_e32 v151, v151, v83, vcc
	ds_add_u32 v160, v162 offset:34416
	ds_add_u32 v161, v163 offset:34416
	s_waitcnt lgkmcnt(6)
	v_pk_add_f32 v[166:167], v[76:77], v[150:151] neg_lo:[0,1] neg_hi:[0,1]
	s_nop 0
	v_pk_fma_f32 v[166:167], v[166:167], v[166:167], v[6:7]
	v_pk_fma_f32 v[80:81], v[112:113], v[20:21], v[16:17] op_sel:[0,1,1]
	v_cmp_eq_u32_sdwa vcc, s17, v41 src0_sel:DWORD src1_sel:BYTE_2
	v_pk_fma_f32 v[80:81], v[114:115], v[36:37], v[80:81] op_sel:[0,1,0]
	v_cvt_pknorm_u16_f32 v158, v156, v157
	v_and_b32_e32 v159, s16, v158
	v_exp_f32_e32 v82, v80
	v_cndmask_b32_e32 v162, v164, v15, vcc
	v_cndmask_b32_e32 v152, 0, v156, vcc
	v_exp_f32_e32 v83, v81
	v_cmp_eq_u32_sdwa vcc, s17, v41 src0_sel:DWORD src1_sel:BYTE_3
	v_lshrrev_b32_sdwa v160, v165, v159 dst_sel:DWORD dst_unused:UNUSED_PAD src0_sel:DWORD src1_sel:WORD_0
	v_lshrrev_b32_sdwa v161, v165, v159 dst_sel:DWORD dst_unused:UNUSED_PAD src0_sel:DWORD src1_sel:WORD_1
	v_cndmask_b32_e32 v163, v164, v15, vcc
	v_cndmask_b32_e32 v153, 0, v157, vcc
	ds_add_u32 v160, v162 offset:1648
	ds_add_u32 v161, v163 offset:1648
	v_pk_fma_f32 v[154:155], v[112:113], v[8:9], v[12:13] op_sel_hi:[1,0,0]
	v_cmp_eq_u32_sdwa vcc, s18, v41 src0_sel:DWORD src1_sel:BYTE_2
	v_pk_fma_f32 v[154:155], v[114:115], v[24:25], v[154:155] op_sel_hi:[1,0,1]
	v_cvt_pknorm_u16_f32 v158, v82, v83
	v_and_b32_e32 v159, s16, v158
	v_exp_f32_e32 v156, v154
	v_cndmask_b32_e32 v162, v164, v15, vcc
	v_cndmask_b32_e32 v152, v152, v82, vcc
	v_exp_f32_e32 v157, v155
	v_cmp_eq_u32_sdwa vcc, s18, v41 src0_sel:DWORD src1_sel:BYTE_3
	v_lshrrev_b32_sdwa v160, v165, v159 dst_sel:DWORD dst_unused:UNUSED_PAD src0_sel:DWORD src1_sel:WORD_0
	v_lshrrev_b32_sdwa v161, v165, v159 dst_sel:DWORD dst_unused:UNUSED_PAD src0_sel:DWORD src1_sel:WORD_1
	v_cndmask_b32_e32 v163, v164, v15, vcc
	v_cndmask_b32_e32 v153, v153, v83, vcc
	ds_add_u32 v160, v162 offset:18032
	ds_add_u32 v161, v163 offset:18032
	v_cmp_eq_u32_sdwa vcc, s19, v41 src0_sel:DWORD src1_sel:BYTE_2
	s_nop 0
	v_cvt_pknorm_u16_f32 v158, v156, v157
	v_and_b32_e32 v159, s16, v158
	v_cndmask_b32_e32 v162, v164, v15, vcc
	v_cndmask_b32_e32 v152, v152, v156, vcc
	v_cmp_eq_u32_sdwa vcc, s19, v41 src0_sel:DWORD src1_sel:BYTE_3
	v_lshrrev_b32_sdwa v160, v165, v159 dst_sel:DWORD dst_unused:UNUSED_PAD src0_sel:DWORD src1_sel:WORD_0
	v_lshrrev_b32_sdwa v161, v165, v159 dst_sel:DWORD dst_unused:UNUSED_PAD src0_sel:DWORD src1_sel:WORD_1
	v_cndmask_b32_e32 v163, v164, v15, vcc
	v_cndmask_b32_e32 v153, v153, v157, vcc
	ds_add_u32 v160, v162 offset:34416
	ds_add_u32 v161, v163 offset:34416
	v_pk_add_f32 v[80:81], v[78:79], v[152:153] neg_lo:[0,1] neg_hi:[0,1]
	s_nop 0
	v_pk_fma_f32 v[6:7], v[80:81], v[80:81], v[166:167]
	ds_read_b128 v[76:79], v1 offset:61440
	v_pk_fma_f32 v[80:81], v[116:117], v[20:21], v[16:17] op_sel_hi:[1,0,0]
	v_pk_fma_f32 v[80:81], v[118:119], v[36:37], v[80:81] op_sel_hi:[1,0,1]
	s_nop 0
	v_exp_f32_e32 v82, v80
	v_exp_f32_e32 v83, v81
	v_pk_fma_f32 v[154:155], v[116:117], v[20:21], v[16:17] op_sel:[0,1,1]
	v_cmp_eq_u32_sdwa vcc, s17, v19 src0_sel:DWORD src1_sel:BYTE_0
	v_pk_fma_f32 v[154:155], v[118:119], v[36:37], v[154:155] op_sel:[0,1,0]
	v_cvt_pknorm_u16_f32 v158, v82, v83
	v_and_b32_e32 v159, s16, v158
	v_exp_f32_e32 v156, v154
	v_cndmask_b32_e32 v162, v164, v15, vcc
	v_cndmask_b32_e32 v150, 0, v82, vcc
	v_exp_f32_e32 v157, v155
	v_cmp_eq_u32_sdwa vcc, s17, v19 src0_sel:DWORD src1_sel:BYTE_1
	v_lshrrev_b32_sdwa v160, v165, v159 dst_sel:DWORD dst_unused:UNUSED_PAD src0_sel:DWORD src1_sel:WORD_0
	v_lshrrev_b32_sdwa v161, v165, v159 dst_sel:DWORD dst_unused:UNUSED_PAD src0_sel:DWORD src1_sel:WORD_1
	v_cndmask_b32_e32 v163, v164, v15, vcc
	v_cndmask_b32_e32 v151, 0, v83, vcc
	ds_add_u32 v160, v162 offset:1648
	ds_add_u32 v161, v163 offset:1648
	v_pk_fma_f32 v[80:81], v[116:117], v[8:9], v[12:13] op_sel_hi:[1,0,0]
	v_cmp_eq_u32_sdwa vcc, s18, v19 src0_sel:DWORD src1_sel:BYTE_0
	v_pk_fma_f32 v[80:81], v[118:119], v[24:25], v[80:81] op_sel_hi:[1,0,1]
	v_cvt_pknorm_u16_f32 v158, v156, v157
	v_and_b32_e32 v159, s16, v158
	v_exp_f32_e32 v82, v80
	v_cndmask_b32_e32 v162, v164, v15, vcc
	v_cndmask_b32_e32 v150, v150, v156, vcc
	v_exp_f32_e32 v83, v81
	v_cmp_eq_u32_sdwa vcc, s18, v19 src0_sel:DWORD src1_sel:BYTE_1
	v_lshrrev_b32_sdwa v160, v165, v159 dst_sel:DWORD dst_unused:UNUSED_PAD src0_sel:DWORD src1_sel:WORD_0
	v_lshrrev_b32_sdwa v161, v165, v159 dst_sel:DWORD dst_unused:UNUSED_PAD src0_sel:DWORD src1_sel:WORD_1
	v_cndmask_b32_e32 v163, v164, v15, vcc
	v_cndmask_b32_e32 v151, v151, v157, vcc
	ds_add_u32 v160, v162 offset:18032
	ds_add_u32 v161, v163 offset:18032
	v_pk_fma_f32 v[154:155], v[120:121], v[20:21], v[16:17] op_sel_hi:[1,0,0]
	v_cmp_eq_u32_sdwa vcc, s19, v19 src0_sel:DWORD src1_sel:BYTE_0
	v_pk_fma_f32 v[154:155], v[122:123], v[36:37], v[154:155] op_sel_hi:[1,0,1]
	v_cvt_pknorm_u16_f32 v158, v82, v83
	v_and_b32_e32 v159, s16, v158
	v_exp_f32_e32 v156, v154
	v_cndmask_b32_e32 v162, v164, v15, vcc
	v_cndmask_b32_e32 v150, v150, v82, vcc
	v_exp_f32_e32 v157, v155
	v_cmp_eq_u32_sdwa vcc, s19, v19 src0_sel:DWORD src1_sel:BYTE_1
	v_lshrrev_b32_sdwa v160, v165, v159 dst_sel:DWORD dst_unused:UNUSED_PAD src0_sel:DWORD src1_sel:WORD_0
	v_lshrrev_b32_sdwa v161, v165, v159 dst_sel:DWORD dst_unused:UNUSED_PAD src0_sel:DWORD src1_sel:WORD_1
	v_cndmask_b32_e32 v163, v164, v15, vcc
	v_cndmask_b32_e32 v151, v151, v83, vcc
	ds_add_u32 v160, v162 offset:34416
	ds_add_u32 v161, v163 offset:34416
	s_waitcnt lgkmcnt(6)
	v_pk_add_f32 v[166:167], v[76:77], v[150:151] neg_lo:[0,1] neg_hi:[0,1]
	s_nop 0
	v_pk_fma_f32 v[166:167], v[166:167], v[166:167], v[6:7]
	v_pk_fma_f32 v[80:81], v[120:121], v[20:21], v[16:17] op_sel:[0,1,1]
	v_cmp_eq_u32_sdwa vcc, s17, v19 src0_sel:DWORD src1_sel:BYTE_2
	v_pk_fma_f32 v[80:81], v[122:123], v[36:37], v[80:81] op_sel:[0,1,0]
	v_cvt_pknorm_u16_f32 v158, v156, v157
	v_and_b32_e32 v159, s16, v158
	v_exp_f32_e32 v82, v80
	v_cndmask_b32_e32 v162, v164, v15, vcc
	v_cndmask_b32_e32 v152, 0, v156, vcc
	v_exp_f32_e32 v83, v81
	v_cmp_eq_u32_sdwa vcc, s17, v19 src0_sel:DWORD src1_sel:BYTE_3
	v_lshrrev_b32_sdwa v160, v165, v159 dst_sel:DWORD dst_unused:UNUSED_PAD src0_sel:DWORD src1_sel:WORD_0
	v_lshrrev_b32_sdwa v161, v165, v159 dst_sel:DWORD dst_unused:UNUSED_PAD src0_sel:DWORD src1_sel:WORD_1
	v_cndmask_b32_e32 v163, v164, v15, vcc
	v_cndmask_b32_e32 v153, 0, v157, vcc
	ds_add_u32 v160, v162 offset:1648
	ds_add_u32 v161, v163 offset:1648
	v_pk_fma_f32 v[154:155], v[120:121], v[8:9], v[12:13] op_sel_hi:[1,0,0]
	v_cmp_eq_u32_sdwa vcc, s18, v19 src0_sel:DWORD src1_sel:BYTE_2
	v_pk_fma_f32 v[154:155], v[122:123], v[24:25], v[154:155] op_sel_hi:[1,0,1]
	v_cvt_pknorm_u16_f32 v158, v82, v83
	v_and_b32_e32 v159, s16, v158
	v_exp_f32_e32 v156, v154
	v_cndmask_b32_e32 v162, v164, v15, vcc
	v_cndmask_b32_e32 v152, v152, v82, vcc
	v_exp_f32_e32 v157, v155
	v_cmp_eq_u32_sdwa vcc, s18, v19 src0_sel:DWORD src1_sel:BYTE_3
	v_lshrrev_b32_sdwa v160, v165, v159 dst_sel:DWORD dst_unused:UNUSED_PAD src0_sel:DWORD src1_sel:WORD_0
	v_lshrrev_b32_sdwa v161, v165, v159 dst_sel:DWORD dst_unused:UNUSED_PAD src0_sel:DWORD src1_sel:WORD_1
	v_cndmask_b32_e32 v163, v164, v15, vcc
	v_cndmask_b32_e32 v153, v153, v83, vcc
	ds_add_u32 v160, v162 offset:18032
	ds_add_u32 v161, v163 offset:18032
	v_cmp_eq_u32_sdwa vcc, s19, v19 src0_sel:DWORD src1_sel:BYTE_2
	s_nop 0
	v_cvt_pknorm_u16_f32 v158, v156, v157
	v_and_b32_e32 v159, s16, v158
	v_cndmask_b32_e32 v162, v164, v15, vcc
	v_cndmask_b32_e32 v152, v152, v156, vcc
	v_cmp_eq_u32_sdwa vcc, s19, v19 src0_sel:DWORD src1_sel:BYTE_3
	v_lshrrev_b32_sdwa v160, v165, v159 dst_sel:DWORD dst_unused:UNUSED_PAD src0_sel:DWORD src1_sel:WORD_0
	v_lshrrev_b32_sdwa v161, v165, v159 dst_sel:DWORD dst_unused:UNUSED_PAD src0_sel:DWORD src1_sel:WORD_1
	v_cndmask_b32_e32 v163, v164, v15, vcc
	v_cndmask_b32_e32 v153, v153, v157, vcc
	ds_add_u32 v160, v162 offset:34416
	ds_add_u32 v161, v163 offset:34416
	v_pk_add_f32 v[80:81], v[78:79], v[152:153] neg_lo:[0,1] neg_hi:[0,1]
	s_nop 0
	v_pk_fma_f32 v[6:7], v[80:81], v[80:81], v[166:167]
	ds_read_b128 v[76:79], v135
	v_pk_fma_f32 v[80:81], v[58:59], v[20:21], v[16:17] op_sel_hi:[1,0,0]
	v_pk_fma_f32 v[80:81], v[124:125], v[36:37], v[80:81] op_sel_hi:[1,0,1]
	s_nop 0
	v_exp_f32_e32 v82, v80
	v_exp_f32_e32 v83, v81
	v_pk_fma_f32 v[154:155], v[58:59], v[20:21], v[16:17] op_sel:[0,1,1]
	v_cmp_eq_u32_sdwa vcc, s17, v13 src0_sel:DWORD src1_sel:BYTE_0
	v_pk_fma_f32 v[154:155], v[124:125], v[36:37], v[154:155] op_sel:[0,1,0]
	v_cvt_pknorm_u16_f32 v158, v82, v83
	v_and_b32_e32 v159, s16, v158
	v_exp_f32_e32 v156, v154
	v_cndmask_b32_e32 v162, v164, v15, vcc
	v_cndmask_b32_e32 v150, 0, v82, vcc
	v_exp_f32_e32 v157, v155
	v_cmp_eq_u32_sdwa vcc, s17, v13 src0_sel:DWORD src1_sel:BYTE_1
	v_lshrrev_b32_sdwa v160, v165, v159 dst_sel:DWORD dst_unused:UNUSED_PAD src0_sel:DWORD src1_sel:WORD_0
	v_lshrrev_b32_sdwa v161, v165, v159 dst_sel:DWORD dst_unused:UNUSED_PAD src0_sel:DWORD src1_sel:WORD_1
	v_cndmask_b32_e32 v163, v164, v15, vcc
	v_cndmask_b32_e32 v151, 0, v83, vcc
	ds_add_u32 v160, v162 offset:1648
	ds_add_u32 v161, v163 offset:1648
	v_pk_fma_f32 v[80:81], v[58:59], v[8:9], v[12:13] op_sel_hi:[1,0,0]
	v_cmp_eq_u32_sdwa vcc, s18, v13 src0_sel:DWORD src1_sel:BYTE_0
	v_pk_fma_f32 v[80:81], v[124:125], v[24:25], v[80:81] op_sel_hi:[1,0,1]
	v_cvt_pknorm_u16_f32 v158, v156, v157
	v_and_b32_e32 v159, s16, v158
	v_exp_f32_e32 v82, v80
	v_cndmask_b32_e32 v162, v164, v15, vcc
	v_cndmask_b32_e32 v150, v150, v156, vcc
	v_exp_f32_e32 v83, v81
	v_cmp_eq_u32_sdwa vcc, s18, v13 src0_sel:DWORD src1_sel:BYTE_1
	v_lshrrev_b32_sdwa v160, v165, v159 dst_sel:DWORD dst_unused:UNUSED_PAD src0_sel:DWORD src1_sel:WORD_0
	v_lshrrev_b32_sdwa v161, v165, v159 dst_sel:DWORD dst_unused:UNUSED_PAD src0_sel:DWORD src1_sel:WORD_1
	v_cndmask_b32_e32 v163, v164, v15, vcc
	v_cndmask_b32_e32 v151, v151, v157, vcc
	ds_add_u32 v160, v162 offset:18032
	ds_add_u32 v161, v163 offset:18032
	v_pk_fma_f32 v[154:155], v[60:61], v[20:21], v[16:17] op_sel_hi:[1,0,0]
	v_cmp_eq_u32_sdwa vcc, s19, v13 src0_sel:DWORD src1_sel:BYTE_0
	v_pk_fma_f32 v[154:155], v[126:127], v[36:37], v[154:155] op_sel_hi:[1,0,1]
	v_cvt_pknorm_u16_f32 v158, v82, v83
	v_and_b32_e32 v159, s16, v158
	v_exp_f32_e32 v156, v154
	v_cndmask_b32_e32 v162, v164, v15, vcc
	v_cndmask_b32_e32 v150, v150, v82, vcc
	v_exp_f32_e32 v157, v155
	v_cmp_eq_u32_sdwa vcc, s19, v13 src0_sel:DWORD src1_sel:BYTE_1
	v_lshrrev_b32_sdwa v160, v165, v159 dst_sel:DWORD dst_unused:UNUSED_PAD src0_sel:DWORD src1_sel:WORD_0
	v_lshrrev_b32_sdwa v161, v165, v159 dst_sel:DWORD dst_unused:UNUSED_PAD src0_sel:DWORD src1_sel:WORD_1
	v_cndmask_b32_e32 v163, v164, v15, vcc
	v_cndmask_b32_e32 v151, v151, v83, vcc
	ds_add_u32 v160, v162 offset:34416
	ds_add_u32 v161, v163 offset:34416
	s_waitcnt lgkmcnt(6)
	v_pk_add_f32 v[166:167], v[76:77], v[150:151] neg_lo:[0,1] neg_hi:[0,1]
	s_nop 0
	v_pk_fma_f32 v[166:167], v[166:167], v[166:167], v[6:7]
	v_pk_fma_f32 v[80:81], v[60:61], v[20:21], v[16:17] op_sel:[0,1,1]
	v_cmp_eq_u32_sdwa vcc, s17, v13 src0_sel:DWORD src1_sel:BYTE_2
	v_pk_fma_f32 v[80:81], v[126:127], v[36:37], v[80:81] op_sel:[0,1,0]
	v_cvt_pknorm_u16_f32 v158, v156, v157
	v_and_b32_e32 v159, s16, v158
	v_exp_f32_e32 v82, v80
	v_cndmask_b32_e32 v162, v164, v15, vcc
	v_cndmask_b32_e32 v152, 0, v156, vcc
	v_exp_f32_e32 v83, v81
	v_cmp_eq_u32_sdwa vcc, s17, v13 src0_sel:DWORD src1_sel:BYTE_3
	v_lshrrev_b32_sdwa v160, v165, v159 dst_sel:DWORD dst_unused:UNUSED_PAD src0_sel:DWORD src1_sel:WORD_0
	v_lshrrev_b32_sdwa v161, v165, v159 dst_sel:DWORD dst_unused:UNUSED_PAD src0_sel:DWORD src1_sel:WORD_1
	v_cndmask_b32_e32 v163, v164, v15, vcc
	v_cndmask_b32_e32 v153, 0, v157, vcc
	ds_add_u32 v160, v162 offset:1648
	ds_add_u32 v161, v163 offset:1648
	v_pk_fma_f32 v[154:155], v[60:61], v[8:9], v[12:13] op_sel_hi:[1,0,0]
	v_cmp_eq_u32_sdwa vcc, s18, v13 src0_sel:DWORD src1_sel:BYTE_2
	v_pk_fma_f32 v[154:155], v[126:127], v[24:25], v[154:155] op_sel_hi:[1,0,1]
	v_cvt_pknorm_u16_f32 v158, v82, v83
	v_and_b32_e32 v159, s16, v158
	v_exp_f32_e32 v156, v154
	v_cndmask_b32_e32 v162, v164, v15, vcc
	v_cndmask_b32_e32 v152, v152, v82, vcc
	v_exp_f32_e32 v157, v155
	v_cmp_eq_u32_sdwa vcc, s18, v13 src0_sel:DWORD src1_sel:BYTE_3
	v_lshrrev_b32_sdwa v160, v165, v159 dst_sel:DWORD dst_unused:UNUSED_PAD src0_sel:DWORD src1_sel:WORD_0
	v_lshrrev_b32_sdwa v161, v165, v159 dst_sel:DWORD dst_unused:UNUSED_PAD src0_sel:DWORD src1_sel:WORD_1
	v_cndmask_b32_e32 v163, v164, v15, vcc
	v_cndmask_b32_e32 v153, v153, v83, vcc
	ds_add_u32 v160, v162 offset:18032
	ds_add_u32 v161, v163 offset:18032
	v_cmp_eq_u32_sdwa vcc, s19, v13 src0_sel:DWORD src1_sel:BYTE_2
	s_nop 0
	v_cvt_pknorm_u16_f32 v158, v156, v157
	v_and_b32_e32 v159, s16, v158
	v_cndmask_b32_e32 v162, v164, v15, vcc
	v_cndmask_b32_e32 v152, v152, v156, vcc
	v_cmp_eq_u32_sdwa vcc, s19, v13 src0_sel:DWORD src1_sel:BYTE_3
	v_lshrrev_b32_sdwa v160, v165, v159 dst_sel:DWORD dst_unused:UNUSED_PAD src0_sel:DWORD src1_sel:WORD_0
	v_lshrrev_b32_sdwa v161, v165, v159 dst_sel:DWORD dst_unused:UNUSED_PAD src0_sel:DWORD src1_sel:WORD_1
	v_cndmask_b32_e32 v163, v164, v15, vcc
	v_cndmask_b32_e32 v153, v153, v157, vcc
	ds_add_u32 v160, v162 offset:34416
	ds_add_u32 v161, v163 offset:34416
	v_pk_add_f32 v[80:81], v[78:79], v[152:153] neg_lo:[0,1] neg_hi:[0,1]
	s_nop 0
	v_pk_fma_f32 v[6:7], v[80:81], v[80:81], v[166:167]
	ds_read_b128 v[76:79], v70
	v_pk_fma_f32 v[80:81], v[62:63], v[20:21], v[16:17] op_sel_hi:[1,0,0]
	v_pk_fma_f32 v[80:81], v[66:67], v[36:37], v[80:81] op_sel_hi:[1,0,1]
	s_nop 0
	v_exp_f32_e32 v82, v80
	v_exp_f32_e32 v83, v81
	v_pk_fma_f32 v[154:155], v[62:63], v[20:21], v[16:17] op_sel:[0,1,1]
	v_cmp_eq_u32_sdwa vcc, s17, v9 src0_sel:DWORD src1_sel:BYTE_0
	v_pk_fma_f32 v[154:155], v[66:67], v[36:37], v[154:155] op_sel:[0,1,0]
	v_cvt_pknorm_u16_f32 v158, v82, v83
	v_and_b32_e32 v159, s16, v158
	v_exp_f32_e32 v156, v154
	v_cndmask_b32_e32 v162, v164, v15, vcc
	v_cndmask_b32_e32 v150, 0, v82, vcc
	v_exp_f32_e32 v157, v155
	v_cmp_eq_u32_sdwa vcc, s17, v9 src0_sel:DWORD src1_sel:BYTE_1
	v_lshrrev_b32_sdwa v160, v165, v159 dst_sel:DWORD dst_unused:UNUSED_PAD src0_sel:DWORD src1_sel:WORD_0
	v_lshrrev_b32_sdwa v161, v165, v159 dst_sel:DWORD dst_unused:UNUSED_PAD src0_sel:DWORD src1_sel:WORD_1
	v_cndmask_b32_e32 v163, v164, v15, vcc
	v_cndmask_b32_e32 v151, 0, v83, vcc
	ds_add_u32 v160, v162 offset:1648
	ds_add_u32 v161, v163 offset:1648
	v_pk_fma_f32 v[80:81], v[62:63], v[8:9], v[12:13] op_sel_hi:[1,0,0]
	v_cmp_eq_u32_sdwa vcc, s18, v9 src0_sel:DWORD src1_sel:BYTE_0
	v_pk_fma_f32 v[80:81], v[66:67], v[24:25], v[80:81] op_sel_hi:[1,0,1]
	v_cvt_pknorm_u16_f32 v158, v156, v157
	v_and_b32_e32 v159, s16, v158
	v_exp_f32_e32 v82, v80
	v_cndmask_b32_e32 v162, v164, v15, vcc
	v_cndmask_b32_e32 v150, v150, v156, vcc
	v_exp_f32_e32 v83, v81
	v_cmp_eq_u32_sdwa vcc, s18, v9 src0_sel:DWORD src1_sel:BYTE_1
	v_lshrrev_b32_sdwa v160, v165, v159 dst_sel:DWORD dst_unused:UNUSED_PAD src0_sel:DWORD src1_sel:WORD_0
	v_lshrrev_b32_sdwa v161, v165, v159 dst_sel:DWORD dst_unused:UNUSED_PAD src0_sel:DWORD src1_sel:WORD_1
	v_cndmask_b32_e32 v163, v164, v15, vcc
	v_cndmask_b32_e32 v151, v151, v157, vcc
	ds_add_u32 v160, v162 offset:18032
	ds_add_u32 v161, v163 offset:18032
	v_pk_fma_f32 v[154:155], v[64:65], v[20:21], v[16:17] op_sel_hi:[1,0,0]
	v_cmp_eq_u32_sdwa vcc, s19, v9 src0_sel:DWORD src1_sel:BYTE_0
	v_pk_fma_f32 v[154:155], v[68:69], v[36:37], v[154:155] op_sel_hi:[1,0,1]
	v_cvt_pknorm_u16_f32 v158, v82, v83
	v_and_b32_e32 v159, s16, v158
	v_exp_f32_e32 v156, v154
	v_cndmask_b32_e32 v162, v164, v15, vcc
	v_cndmask_b32_e32 v150, v150, v82, vcc
	v_exp_f32_e32 v157, v155
	v_cmp_eq_u32_sdwa vcc, s19, v9 src0_sel:DWORD src1_sel:BYTE_1
	v_lshrrev_b32_sdwa v160, v165, v159 dst_sel:DWORD dst_unused:UNUSED_PAD src0_sel:DWORD src1_sel:WORD_0
	v_lshrrev_b32_sdwa v161, v165, v159 dst_sel:DWORD dst_unused:UNUSED_PAD src0_sel:DWORD src1_sel:WORD_1
	v_cndmask_b32_e32 v163, v164, v15, vcc
	v_cndmask_b32_e32 v151, v151, v83, vcc
	ds_add_u32 v160, v162 offset:34416
	ds_add_u32 v161, v163 offset:34416
	s_waitcnt lgkmcnt(6)
	v_pk_add_f32 v[166:167], v[76:77], v[150:151] neg_lo:[0,1] neg_hi:[0,1]
	s_nop 0
	v_pk_fma_f32 v[166:167], v[166:167], v[166:167], v[6:7]
	v_pk_fma_f32 v[80:81], v[64:65], v[20:21], v[16:17] op_sel:[0,1,1]
	v_cmp_eq_u32_sdwa vcc, s17, v9 src0_sel:DWORD src1_sel:BYTE_2
	v_pk_fma_f32 v[80:81], v[68:69], v[36:37], v[80:81] op_sel:[0,1,0]
	v_cvt_pknorm_u16_f32 v158, v156, v157
	v_and_b32_e32 v159, s16, v158
	v_exp_f32_e32 v82, v80
	v_cndmask_b32_e32 v162, v164, v15, vcc
	v_cndmask_b32_e32 v152, 0, v156, vcc
	v_exp_f32_e32 v83, v81
	v_cmp_eq_u32_sdwa vcc, s17, v9 src0_sel:DWORD src1_sel:BYTE_3
	v_lshrrev_b32_sdwa v160, v165, v159 dst_sel:DWORD dst_unused:UNUSED_PAD src0_sel:DWORD src1_sel:WORD_0
	v_lshrrev_b32_sdwa v161, v165, v159 dst_sel:DWORD dst_unused:UNUSED_PAD src0_sel:DWORD src1_sel:WORD_1
	v_cndmask_b32_e32 v163, v164, v15, vcc
	v_cndmask_b32_e32 v153, 0, v157, vcc
	ds_add_u32 v160, v162 offset:1648
	ds_add_u32 v161, v163 offset:1648
	v_pk_fma_f32 v[154:155], v[64:65], v[8:9], v[12:13] op_sel_hi:[1,0,0]
	v_cmp_eq_u32_sdwa vcc, s18, v9 src0_sel:DWORD src1_sel:BYTE_2
	v_pk_fma_f32 v[154:155], v[68:69], v[24:25], v[154:155] op_sel_hi:[1,0,1]
	v_cvt_pknorm_u16_f32 v158, v82, v83
	v_and_b32_e32 v159, s16, v158
	v_exp_f32_e32 v156, v154
	v_cndmask_b32_e32 v162, v164, v15, vcc
	v_cndmask_b32_e32 v152, v152, v82, vcc
	v_exp_f32_e32 v157, v155
	v_cmp_eq_u32_sdwa vcc, s18, v9 src0_sel:DWORD src1_sel:BYTE_3
	v_lshrrev_b32_sdwa v160, v165, v159 dst_sel:DWORD dst_unused:UNUSED_PAD src0_sel:DWORD src1_sel:WORD_0
	v_lshrrev_b32_sdwa v161, v165, v159 dst_sel:DWORD dst_unused:UNUSED_PAD src0_sel:DWORD src1_sel:WORD_1
	v_cndmask_b32_e32 v163, v164, v15, vcc
	v_cndmask_b32_e32 v153, v153, v83, vcc
	ds_add_u32 v160, v162 offset:18032
	ds_add_u32 v161, v163 offset:18032
	v_cmp_eq_u32_sdwa vcc, s19, v9 src0_sel:DWORD src1_sel:BYTE_2
	s_nop 0
	v_cvt_pknorm_u16_f32 v158, v156, v157
	v_and_b32_e32 v159, s16, v158
	v_cndmask_b32_e32 v162, v164, v15, vcc
	v_cndmask_b32_e32 v152, v152, v156, vcc
	v_cmp_eq_u32_sdwa vcc, s19, v9 src0_sel:DWORD src1_sel:BYTE_3
	v_lshrrev_b32_sdwa v160, v165, v159 dst_sel:DWORD dst_unused:UNUSED_PAD src0_sel:DWORD src1_sel:WORD_0
	v_lshrrev_b32_sdwa v161, v165, v159 dst_sel:DWORD dst_unused:UNUSED_PAD src0_sel:DWORD src1_sel:WORD_1
	v_cndmask_b32_e32 v163, v164, v15, vcc
	v_cndmask_b32_e32 v153, v153, v157, vcc
	ds_add_u32 v160, v162 offset:34416
	ds_add_u32 v161, v163 offset:34416
	v_pk_add_f32 v[80:81], v[78:79], v[152:153] neg_lo:[0,1] neg_hi:[0,1]
	s_nop 0
	v_pk_fma_f32 v[6:7], v[80:81], v[80:81], v[166:167]
	s_and_saveexec_b64 s[8:9], s[4:5]
	s_cbranch_execz .LBB0_60
	v_add_u32_e32 v149, 0x18000, v1
	ds_read_b128 v[76:79], v149
	v_pk_fma_f32 v[80:81], v[54:55], v[20:21], v[16:17] op_sel_hi:[1,0,0]
	v_pk_fma_f32 v[80:81], v[50:51], v[36:37], v[80:81] op_sel_hi:[1,0,1]
	s_nop 0
	v_exp_f32_e32 v82, v80
	v_exp_f32_e32 v83, v81
	v_pk_fma_f32 v[154:155], v[54:55], v[20:21], v[16:17] op_sel:[0,1,1]
	v_cmp_eq_u32_sdwa vcc, s17, v40 src0_sel:DWORD src1_sel:BYTE_0
	v_pk_fma_f32 v[154:155], v[50:51], v[36:37], v[154:155] op_sel:[0,1,0]
	v_cvt_pknorm_u16_f32 v158, v82, v83
	v_and_b32_e32 v159, s16, v158
	v_exp_f32_e32 v156, v154
	v_cndmask_b32_e32 v162, v164, v15, vcc
	v_cndmask_b32_e32 v150, 0, v82, vcc
	v_exp_f32_e32 v157, v155
	v_cmp_eq_u32_sdwa vcc, s17, v40 src0_sel:DWORD src1_sel:BYTE_1
	v_lshrrev_b32_sdwa v160, v165, v159 dst_sel:DWORD dst_unused:UNUSED_PAD src0_sel:DWORD src1_sel:WORD_0
	v_lshrrev_b32_sdwa v161, v165, v159 dst_sel:DWORD dst_unused:UNUSED_PAD src0_sel:DWORD src1_sel:WORD_1
	v_cndmask_b32_e32 v163, v164, v15, vcc
	v_cndmask_b32_e32 v151, 0, v83, vcc
	ds_add_u32 v160, v162 offset:1648
	ds_add_u32 v161, v163 offset:1648
	v_pk_fma_f32 v[80:81], v[54:55], v[8:9], v[12:13] op_sel_hi:[1,0,0]
	v_cmp_eq_u32_sdwa vcc, s18, v40 src0_sel:DWORD src1_sel:BYTE_0
	v_pk_fma_f32 v[80:81], v[50:51], v[24:25], v[80:81] op_sel_hi:[1,0,1]
	v_cvt_pknorm_u16_f32 v158, v156, v157
	v_and_b32_e32 v159, s16, v158
	v_exp_f32_e32 v82, v80
	v_cndmask_b32_e32 v162, v164, v15, vcc
	v_cndmask_b32_e32 v150, v150, v156, vcc
	v_exp_f32_e32 v83, v81
	v_cmp_eq_u32_sdwa vcc, s18, v40 src0_sel:DWORD src1_sel:BYTE_1
	v_lshrrev_b32_sdwa v160, v165, v159 dst_sel:DWORD dst_unused:UNUSED_PAD src0_sel:DWORD src1_sel:WORD_0
	v_lshrrev_b32_sdwa v161, v165, v159 dst_sel:DWORD dst_unused:UNUSED_PAD src0_sel:DWORD src1_sel:WORD_1
	v_cndmask_b32_e32 v163, v164, v15, vcc
	v_cndmask_b32_e32 v151, v151, v157, vcc
	ds_add_u32 v160, v162 offset:18032
	ds_add_u32 v161, v163 offset:18032
	v_pk_fma_f32 v[154:155], v[46:47], v[20:21], v[16:17] op_sel_hi:[1,0,0]
	v_cmp_eq_u32_sdwa vcc, s19, v40 src0_sel:DWORD src1_sel:BYTE_0
	v_pk_fma_f32 v[154:155], v[74:75], v[36:37], v[154:155] op_sel_hi:[1,0,1]
	v_cvt_pknorm_u16_f32 v158, v82, v83
	v_and_b32_e32 v159, s16, v158
	v_exp_f32_e32 v156, v154
	v_cndmask_b32_e32 v162, v164, v15, vcc
	v_cndmask_b32_e32 v150, v150, v82, vcc
	v_exp_f32_e32 v157, v155
	v_cmp_eq_u32_sdwa vcc, s19, v40 src0_sel:DWORD src1_sel:BYTE_1
	v_lshrrev_b32_sdwa v160, v165, v159 dst_sel:DWORD dst_unused:UNUSED_PAD src0_sel:DWORD src1_sel:WORD_0
	v_lshrrev_b32_sdwa v161, v165, v159 dst_sel:DWORD dst_unused:UNUSED_PAD src0_sel:DWORD src1_sel:WORD_1
	v_cndmask_b32_e32 v163, v164, v15, vcc
	v_cndmask_b32_e32 v151, v151, v83, vcc
	ds_add_u32 v160, v162 offset:34416
	ds_add_u32 v161, v163 offset:34416
	s_waitcnt lgkmcnt(6)
	v_pk_add_f32 v[166:167], v[76:77], v[150:151] neg_lo:[0,1] neg_hi:[0,1]
	s_nop 0
	v_pk_fma_f32 v[166:167], v[166:167], v[166:167], v[6:7]
	v_pk_fma_f32 v[80:81], v[46:47], v[20:21], v[16:17] op_sel:[0,1,1]
	v_cmp_eq_u32_sdwa vcc, s17, v40 src0_sel:DWORD src1_sel:BYTE_2
	v_pk_fma_f32 v[80:81], v[74:75], v[36:37], v[80:81] op_sel:[0,1,0]
	v_cvt_pknorm_u16_f32 v158, v156, v157
	v_and_b32_e32 v159, s16, v158
	v_exp_f32_e32 v82, v80
	v_cndmask_b32_e32 v162, v164, v15, vcc
	v_cndmask_b32_e32 v152, 0, v156, vcc
	v_exp_f32_e32 v83, v81
	v_cmp_eq_u32_sdwa vcc, s17, v40 src0_sel:DWORD src1_sel:BYTE_3
	v_lshrrev_b32_sdwa v160, v165, v159 dst_sel:DWORD dst_unused:UNUSED_PAD src0_sel:DWORD src1_sel:WORD_0
	v_lshrrev_b32_sdwa v161, v165, v159 dst_sel:DWORD dst_unused:UNUSED_PAD src0_sel:DWORD src1_sel:WORD_1
	v_cndmask_b32_e32 v163, v164, v15, vcc
	v_cndmask_b32_e32 v153, 0, v157, vcc
	ds_add_u32 v160, v162 offset:1648
	ds_add_u32 v161, v163 offset:1648
	v_pk_fma_f32 v[154:155], v[46:47], v[8:9], v[12:13] op_sel_hi:[1,0,0]
	v_cmp_eq_u32_sdwa vcc, s18, v40 src0_sel:DWORD src1_sel:BYTE_2
	v_pk_fma_f32 v[154:155], v[74:75], v[24:25], v[154:155] op_sel_hi:[1,0,1]
	v_cvt_pknorm_u16_f32 v158, v82, v83
	v_and_b32_e32 v159, s16, v158
	v_exp_f32_e32 v156, v154
	v_cndmask_b32_e32 v162, v164, v15, vcc
	v_cndmask_b32_e32 v152, v152, v82, vcc
	v_exp_f32_e32 v157, v155
	v_cmp_eq_u32_sdwa vcc, s18, v40 src0_sel:DWORD src1_sel:BYTE_3
	v_lshrrev_b32_sdwa v160, v165, v159 dst_sel:DWORD dst_unused:UNUSED_PAD src0_sel:DWORD src1_sel:WORD_0
	v_lshrrev_b32_sdwa v161, v165, v159 dst_sel:DWORD dst_unused:UNUSED_PAD src0_sel:DWORD src1_sel:WORD_1
	v_cndmask_b32_e32 v163, v164, v15, vcc
	v_cndmask_b32_e32 v153, v153, v83, vcc
	ds_add_u32 v160, v162 offset:18032
	ds_add_u32 v161, v163 offset:18032
	v_cmp_eq_u32_sdwa vcc, s19, v40 src0_sel:DWORD src1_sel:BYTE_2
	s_nop 0
	v_cvt_pknorm_u16_f32 v158, v156, v157
	v_and_b32_e32 v159, s16, v158
	v_cndmask_b32_e32 v162, v164, v15, vcc
	v_cndmask_b32_e32 v152, v152, v156, vcc
	v_cmp_eq_u32_sdwa vcc, s19, v40 src0_sel:DWORD src1_sel:BYTE_3
	v_lshrrev_b32_sdwa v160, v165, v159 dst_sel:DWORD dst_unused:UNUSED_PAD src0_sel:DWORD src1_sel:WORD_0
	v_lshrrev_b32_sdwa v161, v165, v159 dst_sel:DWORD dst_unused:UNUSED_PAD src0_sel:DWORD src1_sel:WORD_1
	v_cndmask_b32_e32 v163, v164, v15, vcc
	v_cndmask_b32_e32 v153, v153, v157, vcc
	ds_add_u32 v160, v162 offset:34416
	ds_add_u32 v161, v163 offset:34416
	v_pk_add_f32 v[80:81], v[78:79], v[152:153] neg_lo:[0,1] neg_hi:[0,1]
	s_nop 0
	v_pk_fma_f32 v[6:7], v[80:81], v[80:81], v[166:167]
